# attention loop: row-sum and row-max chains split into two independent interleaved chains (same op count), s_nop before sum permlane dropped, max permlane wait states filled with independent ops
# baseline (speedup 1.0000x reference)
.LBB0_787:
	s_mov_b32 s54, s0
	s_add_i32 s55, s28, -3
	s_lshl_b32 s21, s0, 14
	v_add_u32_e32 v180, s21, v191
	v_add_u32_e32 v84, v180, v190
	ds_read_b128 v[80:83], v84 offset:50176
	ds_read_b128 v[84:87], v84 offset:58368
	v_add_u32_e32 v195, v180, v188
	ds_read_b128 v[196:199], v195 offset:50176
	ds_read_b128 v[200:203], v195 offset:58368
	v_add_u32_e32 v195, v180, v187
	s_waitcnt lgkmcnt(3)
	v_mfma_f32_32x32x16_bf16 v[96:111], v[80:83], v[122:125], 0
	v_add_u32_e32 v180, v180, v186
	v_exp_f32_e32 v204, v72
	v_exp_f32_e32 v205, v73
	v_exp_f32_e32 v206, v74
	v_exp_f32_e32 v207, v75
	v_exp_f32_e32 v208, v76
	v_exp_f32_e32 v209, v77
	s_waitcnt lgkmcnt(2)
	v_mfma_f32_32x32x16_bf16 v[80:95], v[84:87], v[122:125], 0
	v_exp_f32_e32 v210, v78
	v_exp_f32_e32 v79, v79
	s_waitcnt lgkmcnt(1)
	v_mfma_f32_32x32x16_bf16 v[96:111], v[196:199], v[126:129], v[96:111]
	s_waitcnt lgkmcnt(0)
	v_mfma_f32_32x32x16_bf16 v[80:95], v[200:203], v[126:129], v[80:95]
	ds_read_b128 v[196:199], v195 offset:50176
	ds_read_b128 v[200:203], v195 offset:58368
	s_waitcnt lgkmcnt(1)
	v_mfma_f32_32x32x16_bf16 v[96:111], v[196:199], v[118:121], v[96:111]
	s_waitcnt lgkmcnt(0)
	v_mfma_f32_32x32x16_bf16 v[80:95], v[200:203], v[118:121], v[80:95]
	ds_read_b128 v[196:199], v180 offset:50176
	ds_read_b128 v[200:203], v180 offset:58368
	v_exp_f32_e32 v180, v64
	v_add_f32_e32 v64, v161, v159
	v_add_f32_e32 v195, v157, v160
	v_add_f32_e32 v64, v155, v64
	v_add_f32_e32 v195, v158, v195
	v_add_f32_e32 v64, v154, v64
	v_add_f32_e32 v195, v156, v195
	v_add_f32_e32 v64, v151, v64
	v_add_f32_e32 v195, v153, v195
	v_add_f32_e32 v64, v149, v64
	v_add_f32_e32 v195, v152, v195
	v_add_f32_e32 v64, v147, v64
	s_waitcnt lgkmcnt(1)
	v_mfma_f32_32x32x16_bf16 v[96:111], v[196:199], v[114:117], v[96:111]
	v_exp_f32_e32 v197, v65
	v_add_f32_e32 v195, v150, v195
	v_exp_f32_e32 v198, v66
	v_add_f32_e32 v64, v146, v64
	v_exp_f32_e32 v199, v67
	v_add_f32_e32 v195, v148, v195
	v_add_f32_e32 v64, v180, v64
	s_waitcnt lgkmcnt(0)
	v_mfma_f32_32x32x16_bf16 v[80:95], v[200:203], v[114:117], v[80:95]
	v_exp_f32_e32 v200, v68
	v_exp_f32_e32 v201, v69
	v_add_f32_e32 v195, v197, v195
	v_exp_f32_e32 v202, v70
	v_add_f32_e32 v64, v198, v64
	v_exp_f32_e32 v203, v71
	v_add_f32_e32 v195, v199, v195
	v_add_f32_e32 v64, v200, v64
	v_add_f32_e32 v195, v201, v195
	v_add_f32_e32 v64, v202, v64
	v_add_f32_e32 v195, v203, v195
	v_add_f32_e32 v64, v204, v64
	v_add_f32_e32 v195, v205, v195
	v_add_f32_e32 v64, v206, v64
	v_add_f32_e32 v195, v207, v195
	v_add_f32_e32 v64, v208, v64
	v_add_f32_e32 v195, v209, v195
	v_add_f32_e32 v64, v210, v64
	v_add_f32_e32 v195, v79, v195
	v_add_f32_e32 v195, v195, v64
	v_mov_b32_e32 v196, v195
	v_cvt_pk_bf16_f32 v64, v159, v161
	v_cvt_pk_bf16_f32 v65, v157, v160
	v_cvt_pk_bf16_f32 v66, v155, v158
	v_permlane32_swap_b32_e32 v195, v196
	v_cvt_pk_bf16_f32 v67, v154, v156
	v_permlane32_swap_b32_e32 v64, v66
	v_cvt_pk_bf16_f32 v68, v151, v153
	v_cvt_pk_bf16_f32 v69, v149, v152
	v_cvt_pk_bf16_f32 v70, v147, v150
	v_cvt_pk_bf16_f32 v71, v146, v148
	v_cvt_pk_bf16_f32 v72, v180, v197
	v_cvt_pk_bf16_f32 v73, v198, v199
	v_cvt_pk_bf16_f32 v74, v200, v201
	v_cvt_pk_bf16_f32 v75, v202, v203
	v_cvt_pk_bf16_f32 v76, v204, v205
	v_cvt_pk_bf16_f32 v77, v206, v207
	v_cvt_pk_bf16_f32 v78, v208, v209
	v_cvt_pk_bf16_f32 v79, v210, v79
	v_permlane32_swap_b32_e32 v65, v67
	v_permlane32_swap_b32_e32 v68, v70
	v_permlane32_swap_b32_e32 v69, v71
	v_permlane32_swap_b32_e32 v72, v74
	v_permlane32_swap_b32_e32 v73, v75
	v_permlane32_swap_b32_e32 v76, v78
	v_permlane32_swap_b32_e32 v77, v79
	s_cmp_lt_u32 s55, 30
	s_cselect_b32 s0, 0, 0xffffffe0
	s_cselect_b32 s1, s18, s16
	s_add_i32 s0, s0, s28
	s_lshl_b32 s0, s0, 6
	s_add_i32 s0, s0, s1
	s_sub_i32 s0, s0, 64
	s_mul_i32 s64, s0, 0x1800
	s_add_u32 s66, s8, s96
	s_addc_u32 s67, s9, 0
	s_add_u32 s66, s66, s64
	s_addc_u32 s67, s67, 0
	s_add_u32 s68, s66, 0x30000
	s_addc_u32 s69, s67, 0
	s_add_u32 s70, s6, s96
	s_addc_u32 s71, s7, 0
	s_add_u32 s70, s70, s64
	s_addc_u32 s71, s71, 0
	s_add_u32 s72, s70, 0x30000
	s_addc_u32 s73, s71, 0
	global_load_dwordx4 v[146:149], v241, s[66:67]
	global_load_dwordx4 v[150:153], v241, s[68:69]
	global_load_dwordx4 v[154:157], v241, s[70:71]
	global_load_dwordx4 v[158:161], v241, s[72:73]
	s_lshl_b32 s20, s29, 14
	v_add_u32_e32 v180, s20, v194
	ds_read_b64_tr_b16 v[198:199], v180 offset:0
	ds_read_b64_tr_b16 v[200:201], v180 offset:0x800
	ds_read_b64_tr_b16 v[202:203], v180 offset:0x1000
	ds_read_b64_tr_b16 v[204:205], v180 offset:0x1800
	ds_read_b64_tr_b16 v[206:207], v180 offset:0x2000
	ds_read_b64_tr_b16 v[208:209], v180 offset:0x2800
	ds_read_b64_tr_b16 v[222:223], v180 offset:0x3000
	ds_read_b64_tr_b16 v[224:225], v180 offset:0x3800
	s_waitcnt lgkmcnt(0)
	s_nop 0
	v_mfma_f32_32x32x16_bf16 v[0:15], v[64:67], v[198:201], v[0:15]
	ds_read_b64_tr_b16 v[198:199], v180 offset:0x200
	ds_read_b64_tr_b16 v[200:201], v180 offset:0xa00
	v_mfma_f32_32x32x16_bf16 v[0:15], v[68:71], v[202:205], v[0:15]
	ds_read_b64_tr_b16 v[202:203], v180 offset:0x1200
	ds_read_b64_tr_b16 v[204:205], v180 offset:0x1a00
	v_mfma_f32_32x32x16_bf16 v[0:15], v[72:75], v[206:209], v[0:15]
	ds_read_b64_tr_b16 v[206:207], v180 offset:0x2200
	ds_read_b64_tr_b16 v[208:209], v180 offset:0x2a00
	v_mfma_f32_32x32x16_bf16 v[0:15], v[76:79], v[222:225], v[0:15]
	ds_read_b64_tr_b16 v[222:223], v180 offset:0x3200
	ds_read_b64_tr_b16 v[224:225], v180 offset:0x3a00
	s_waitcnt lgkmcnt(0)
	v_mfma_f32_32x32x16_bf16 v[48:63], v[64:67], v[198:201], v[48:63]
	ds_read_b64_tr_b16 v[198:199], v180 offset:0x400
	ds_read_b64_tr_b16 v[200:201], v180 offset:0xc00
	v_mfma_f32_32x32x16_bf16 v[48:63], v[68:71], v[202:205], v[48:63]
	ds_read_b64_tr_b16 v[202:203], v180 offset:0x1400
	ds_read_b64_tr_b16 v[204:205], v180 offset:0x1c00
	v_mfma_f32_32x32x16_bf16 v[48:63], v[72:75], v[206:209], v[48:63]
	ds_read_b64_tr_b16 v[206:207], v180 offset:0x2400
	ds_read_b64_tr_b16 v[208:209], v180 offset:0x2c00
	v_mfma_f32_32x32x16_bf16 v[48:63], v[76:79], v[222:225], v[48:63]
	ds_read_b64_tr_b16 v[222:223], v180 offset:0x3400
	ds_read_b64_tr_b16 v[224:225], v180 offset:0x3c00
	s_waitcnt lgkmcnt(0)
	v_mfma_f32_32x32x16_bf16 v[32:47], v[64:67], v[198:201], v[32:47]
	ds_read_b64_tr_b16 v[198:199], v180 offset:0x600
	ds_read_b64_tr_b16 v[200:201], v180 offset:0xe00
	v_mfma_f32_32x32x16_bf16 v[32:47], v[68:71], v[202:205], v[32:47]
	ds_read_b64_tr_b16 v[202:203], v180 offset:0x1600
	ds_read_b64_tr_b16 v[204:205], v180 offset:0x1e00
	v_mfma_f32_32x32x16_bf16 v[32:47], v[72:75], v[206:209], v[32:47]
	ds_read_b64_tr_b16 v[206:207], v180 offset:0x2600
	ds_read_b64_tr_b16 v[208:209], v180 offset:0x2e00
	v_mfma_f32_32x32x16_bf16 v[32:47], v[76:79], v[222:225], v[32:47]
	ds_read_b64_tr_b16 v[222:223], v180 offset:0x3600
	ds_read_b64_tr_b16 v[224:225], v180 offset:0x3e00
	s_waitcnt lgkmcnt(0)
	v_mfma_f32_32x32x16_bf16 v[16:31], v[64:67], v[198:201], v[16:31]
	v_max_f32_e32 v64, v96, v97
	v_max3_f32 v65, v80, v81, v82
	v_max3_f32 v64, v64, v98, v99
	v_max3_f32 v65, v65, v83, v84
	v_max3_f32 v64, v64, v100, v101
	v_mfma_f32_32x32x16_bf16 v[16:31], v[68:71], v[202:205], v[16:31]
	v_max3_f32 v65, v65, v85, v86
	v_max3_f32 v64, v64, v102, v103
	v_max3_f32 v65, v65, v87, v88
	v_max3_f32 v64, v64, v104, v105
	v_max3_f32 v65, v65, v89, v90
	v_max3_f32 v64, v64, v106, v107
	v_max3_f32 v65, v65, v91, v92
	v_mfma_f32_32x32x16_bf16 v[16:31], v[72:75], v[206:209], v[16:31]
	v_max3_f32 v64, v64, v108, v109
	v_max3_f32 v65, v65, v93, v94
	v_max3_f32 v64, v64, v110, v111
	v_max3_f32 v64, v64, v65, v95
	v_mov_b32_e32 v65, v64
	v_cmp_eq_f32_e32 vcc, 0, v164
	v_mov_b32_e32 v198, 1.0
	v_permlane32_swap_b32_e32 v64, v65
	v_mfma_f32_32x32x16_bf16 v[16:31], v[76:79], v[222:225], v[16:31]
	v_max_f32_e32 v64, v64, v65
	v_cmp_ge_f32_e64 s[40:41], s75, v64
	s_and_b64 s[0:1], vcc, s[40:41]
	s_cmp_eq_u64 s[0:1], exec
	s_cbranch_scc0 .LBB0_801

.LBB0_792:
	v_exp_f32_e32 v197, v96
	v_exp_f32_e32 v208, v97
	v_exp_f32_e32 v209, v98
	v_exp_f32_e32 v210, v99
	v_exp_f32_e32 v211, v100
	v_exp_f32_e32 v220, v101
	v_exp_f32_e32 v221, v102
	v_exp_f32_e32 v222, v103
	v_exp_f32_e32 v223, v104
	v_exp_f32_e32 v224, v105
	v_exp_f32_e32 v225, v106
	v_exp_f32_e32 v226, v107
	v_exp_f32_e32 v227, v108
	v_exp_f32_e32 v228, v109
	v_exp_f32_e32 v229, v110
	v_exp_f32_e32 v230, v111
	s_waitcnt lgkmcnt(0)
	s_barrier
	v_add_u32_e32 v199, s22, v189
	v_add_u32_e32 v68, v199, v190
	ds_read_b128 v[64:67], v68 offset:50176
	ds_read_b128 v[68:71], v68 offset:58368
	v_add_u32_e32 v204, v199, v188
	ds_read_b128 v[200:203], v204 offset:50176
	ds_read_b128 v[204:207], v204 offset:58368
	v_exp_f32_e32 v231, v87
	s_waitcnt lgkmcnt(3)
	v_mfma_f32_32x32x16_bf16 v[96:111], v[64:67], v[122:125], 0
	v_exp_f32_e32 v232, v88
	v_exp_f32_e32 v233, v89
	v_exp_f32_e32 v234, v90
	v_exp_f32_e32 v235, v91
	v_exp_f32_e32 v236, v92
	v_exp_f32_e32 v237, v93
	v_exp_f32_e32 v238, v94
	s_waitcnt lgkmcnt(2)
	v_mfma_f32_32x32x16_bf16 v[64:79], v[68:71], v[122:125], 0
	v_exp_f32_e32 v95, v95
	s_waitcnt lgkmcnt(1)
	v_mfma_f32_32x32x16_bf16 v[96:111], v[200:203], v[126:129], v[96:111]
	s_waitcnt lgkmcnt(0)
	v_mfma_f32_32x32x16_bf16 v[64:79], v[204:207], v[126:129], v[64:79]
	v_add_u32_e32 v204, v199, v187
	ds_read_b128 v[200:203], v204 offset:50176
	ds_read_b128 v[204:207], v204 offset:58368
	v_add_u32_e32 v199, v199, v186
	s_waitcnt lgkmcnt(1)
	v_mfma_f32_32x32x16_bf16 v[96:111], v[200:203], v[118:121], v[96:111]
	s_waitcnt lgkmcnt(0)
	v_mfma_f32_32x32x16_bf16 v[64:79], v[204:207], v[118:121], v[64:79]
	ds_read_b128 v[200:203], v199 offset:50176
	ds_read_b128 v[204:207], v199 offset:58368
	s_waitcnt lgkmcnt(1)
	v_mfma_f32_32x32x16_bf16 v[96:111], v[200:203], v[114:117], v[96:111]
	v_exp_f32_e32 v201, v80
	v_add_f32_e32 v80, v208, v197
	v_add_f32_e32 v199, v209, v210
	v_add_f32_e32 v80, v211, v80
	v_add_f32_e32 v199, v220, v199
	v_add_f32_e32 v80, v221, v80
	v_add_f32_e32 v199, v222, v199
	v_add_f32_e32 v80, v223, v80
	v_add_f32_e32 v199, v224, v199
	v_add_f32_e32 v80, v225, v80
	v_add_f32_e32 v199, v226, v199
	v_add_f32_e32 v80, v227, v80
	v_exp_f32_e32 v202, v81
	v_add_f32_e32 v199, v228, v199
	v_exp_f32_e32 v203, v82
	v_add_f32_e32 v80, v229, v80
	s_waitcnt lgkmcnt(0)
	v_mfma_f32_32x32x16_bf16 v[64:79], v[204:207], v[114:117], v[64:79]
	v_exp_f32_e32 v204, v83
	v_add_f32_e32 v199, v230, v199
	v_exp_f32_e32 v205, v84
	v_add_f32_e32 v80, v201, v80
	v_exp_f32_e32 v206, v85
	v_add_f32_e32 v199, v202, v199
	v_exp_f32_e32 v207, v86
	v_add_f32_e32 v80, v203, v80
	v_add_f32_e32 v199, v204, v199
	v_add_f32_e32 v80, v205, v80
	v_add_f32_e32 v199, v206, v199
	v_add_f32_e32 v80, v207, v80
	v_add_f32_e32 v199, v231, v199
	v_add_f32_e32 v80, v232, v80
	v_add_f32_e32 v199, v233, v199
	v_add_f32_e32 v80, v234, v80
	v_add_f32_e32 v199, v235, v199
	v_add_f32_e32 v80, v236, v80
	v_add_f32_e32 v199, v237, v199
	v_add_f32_e32 v80, v238, v80
	v_add_f32_e32 v199, v95, v199
	v_add_f32_e32 v199, v199, v80
	v_mov_b32_e32 v200, v199
	v_cvt_pk_bf16_f32 v80, v197, v208
	v_cvt_pk_bf16_f32 v81, v209, v210
	v_cvt_pk_bf16_f32 v82, v211, v220
	v_cvt_pk_bf16_f32 v83, v221, v222
	v_cvt_pk_bf16_f32 v84, v223, v224
	v_cvt_pk_bf16_f32 v85, v225, v226
	v_cvt_pk_bf16_f32 v86, v227, v228
	v_cvt_pk_bf16_f32 v87, v229, v230
	v_cvt_pk_bf16_f32 v88, v201, v202
	v_cvt_pk_bf16_f32 v89, v203, v204
	v_cvt_pk_bf16_f32 v90, v205, v206
	v_cvt_pk_bf16_f32 v91, v207, v231
	v_cvt_pk_bf16_f32 v92, v232, v233
	v_cvt_pk_bf16_f32 v93, v234, v235
	v_cvt_pk_bf16_f32 v94, v236, v237
	v_cvt_pk_bf16_f32 v95, v238, v95
	v_permlane32_swap_b32_e32 v199, v200
	v_permlane32_swap_b32_e32 v80, v82
	v_permlane32_swap_b32_e32 v81, v83
	v_permlane32_swap_b32_e32 v84, v86
	v_permlane32_swap_b32_e32 v85, v87
	v_permlane32_swap_b32_e32 v88, v90
	v_permlane32_swap_b32_e32 v89, v91
	v_permlane32_swap_b32_e32 v92, v94
	v_permlane32_swap_b32_e32 v93, v95
	s_cmp_gt_u32 s55, 32
	s_cbranch_scc1 .LBB0_794
	s_cmp_lt_u32 s55, 29
	s_cselect_b32 s0, 0, 0xffffffe0
	s_cselect_b32 s1, s18, s16
	s_add_i32 s0, s0, s28
	s_lshl_b32 s0, s0, 6
	s_add_i32 s0, s0, s1
	s_mul_i32 s64, s0, 0x1800
	s_add_u32 s66, s8, s96
	s_addc_u32 s67, s9, 0
	s_add_u32 s66, s66, s64
	s_addc_u32 s67, s67, 0
	s_add_u32 s68, s66, 0x30000
	s_addc_u32 s69, s67, 0
	s_add_u32 s70, s6, s96
	s_addc_u32 s71, s7, 0
	s_add_u32 s70, s70, s64
	s_addc_u32 s71, s71, 0
	s_add_u32 s72, s70, 0x30000
	s_addc_u32 s73, s71, 0
	global_load_dwordx4 v[130:133], v241, s[66:67]
	global_load_dwordx4 v[134:137], v241, s[68:69]
	global_load_dwordx4 v[138:141], v241, s[70:71]
	global_load_dwordx4 v[142:145], v241, s[72:73]
.LBB0_794:
	v_add_u32_e32 v197, s21, v194
	ds_read_b64_tr_b16 v[202:203], v197 offset:0
	ds_read_b64_tr_b16 v[204:205], v197 offset:0x800
	ds_read_b64_tr_b16 v[206:207], v197 offset:0x1000
	ds_read_b64_tr_b16 v[208:209], v197 offset:0x1800
	ds_read_b64_tr_b16 v[222:223], v197 offset:0x2000
	ds_read_b64_tr_b16 v[224:225], v197 offset:0x2800
	ds_read_b64_tr_b16 v[226:227], v197 offset:0x3000
	ds_read_b64_tr_b16 v[228:229], v197 offset:0x3800
	s_waitcnt lgkmcnt(0)
	s_nop 0
	v_mfma_f32_32x32x16_bf16 v[0:15], v[80:83], v[202:205], v[0:15]
	ds_read_b64_tr_b16 v[202:203], v197 offset:0x200
	ds_read_b64_tr_b16 v[204:205], v197 offset:0xa00
	v_mfma_f32_32x32x16_bf16 v[0:15], v[84:87], v[206:209], v[0:15]
	ds_read_b64_tr_b16 v[206:207], v197 offset:0x1200
	ds_read_b64_tr_b16 v[208:209], v197 offset:0x1a00
	v_mfma_f32_32x32x16_bf16 v[0:15], v[88:91], v[222:225], v[0:15]
	ds_read_b64_tr_b16 v[222:223], v197 offset:0x2200
	ds_read_b64_tr_b16 v[224:225], v197 offset:0x2a00
	v_mfma_f32_32x32x16_bf16 v[0:15], v[92:95], v[226:229], v[0:15]
	ds_read_b64_tr_b16 v[226:227], v197 offset:0x3200
	ds_read_b64_tr_b16 v[228:229], v197 offset:0x3a00
	s_waitcnt lgkmcnt(0)
	v_mfma_f32_32x32x16_bf16 v[48:63], v[80:83], v[202:205], v[48:63]
	ds_read_b64_tr_b16 v[202:203], v197 offset:0x400
	ds_read_b64_tr_b16 v[204:205], v197 offset:0xc00
	v_mfma_f32_32x32x16_bf16 v[48:63], v[84:87], v[206:209], v[48:63]
	ds_read_b64_tr_b16 v[206:207], v197 offset:0x1400
	ds_read_b64_tr_b16 v[208:209], v197 offset:0x1c00
	v_mfma_f32_32x32x16_bf16 v[48:63], v[88:91], v[222:225], v[48:63]
	ds_read_b64_tr_b16 v[222:223], v197 offset:0x2400
	ds_read_b64_tr_b16 v[224:225], v197 offset:0x2c00
	v_mfma_f32_32x32x16_bf16 v[48:63], v[92:95], v[226:229], v[48:63]
	ds_read_b64_tr_b16 v[226:227], v197 offset:0x3400
	ds_read_b64_tr_b16 v[228:229], v197 offset:0x3c00
	s_waitcnt lgkmcnt(0)
	v_mfma_f32_32x32x16_bf16 v[32:47], v[80:83], v[202:205], v[32:47]
	ds_read_b64_tr_b16 v[202:203], v197 offset:0x600
	ds_read_b64_tr_b16 v[204:205], v197 offset:0xe00
	v_mfma_f32_32x32x16_bf16 v[32:47], v[84:87], v[206:209], v[32:47]
	ds_read_b64_tr_b16 v[206:207], v197 offset:0x1600
	ds_read_b64_tr_b16 v[208:209], v197 offset:0x1e00
	v_mfma_f32_32x32x16_bf16 v[32:47], v[88:91], v[222:225], v[32:47]
	ds_read_b64_tr_b16 v[222:223], v197 offset:0x2600
	ds_read_b64_tr_b16 v[224:225], v197 offset:0x2e00
	v_mfma_f32_32x32x16_bf16 v[32:47], v[92:95], v[226:229], v[32:47]
	ds_read_b64_tr_b16 v[226:227], v197 offset:0x3600
	ds_read_b64_tr_b16 v[228:229], v197 offset:0x3e00
	s_waitcnt lgkmcnt(0)
	v_mfma_f32_32x32x16_bf16 v[16:31], v[80:83], v[202:205], v[16:31]
	v_max_f32_e32 v80, v96, v97
	v_max3_f32 v81, v64, v65, v66
	v_max3_f32 v80, v80, v98, v99
	v_max3_f32 v81, v81, v67, v68
	v_max3_f32 v80, v80, v100, v101
	v_mfma_f32_32x32x16_bf16 v[16:31], v[84:87], v[206:209], v[16:31]
	v_max3_f32 v81, v81, v69, v70
	v_max3_f32 v80, v80, v102, v103
	v_max3_f32 v81, v81, v71, v72
	v_max3_f32 v80, v80, v104, v105
	v_max3_f32 v81, v81, v73, v74
	v_max3_f32 v80, v80, v106, v107
	v_max3_f32 v81, v81, v75, v76
	v_mfma_f32_32x32x16_bf16 v[16:31], v[88:91], v[222:225], v[16:31]
	v_max3_f32 v80, v80, v108, v109
	v_max3_f32 v81, v81, v77, v78
	v_max3_f32 v80, v80, v110, v111
	v_max3_f32 v80, v80, v81, v79
	v_mov_b32_e32 v81, v80
	v_cmp_eq_f32_e32 vcc, 0, v164
	v_mov_b32_e32 v197, 1.0
	v_permlane32_swap_b32_e32 v80, v81
	v_mfma_f32_32x32x16_bf16 v[16:31], v[92:95], v[226:229], v[16:31]
	v_max_f32_e32 v80, v80, v81
	v_cmp_ge_f32_e64 s[40:41], s75, v80
	s_and_b64 s[0:1], vcc, s[40:41]
	s_cmp_eq_u64 s[0:1], exec
	s_cbranch_scc0 .LBB0_802
